# s17 + bias-row address select in the attention loops via v_bfe_i32 + v_bfi_b32 (no VCC round trip, no hazard nop)
# speedup vs baseline: 1.0049x; 1.0049x over previous
; #define WAIT_BAR(N) asm volatile("s_waitcnt vmcnt(" #N ") lgkmcnt(0)\n\ts_barrier" ::: "memory")
; #define RESC() do { if (resc) { asm volatile("s_waitcnt lgkmcnt(0)" ::: "memory"); \
;       _Pragma("unroll") for (int d_ = 0; d_ < 2; ++d_) _Pragma("unroll") for (int r = 0; r < 16; ++r) o[d_][r] *= wsf[crow(r, hi)]; } } while (0)
; #define ROT() do { sl_prev = sl_cur; sl_cur = sl_next; sl_next = (sl_next == (NSLOT - 1) * SLOTB) ? 0 : sl_next + SLOTB; } while (0)
; template <bool MOBA, int THRL> ...
;     ...
;     bool resc = false;
;     ...
;     int t = 1;
;     ...
;     for (; t + 5 < NT; t += 2) {
;         STEP(pB0, pB1, pA0, pA1, t, true, true, true);       WAIT_BAR(2); RESC(); ROT();
.LBB0_480:
	v_lshl_add_u32 v68, s18, 8, v234
	s_ashr_i32 s18, s18, 2
	v_bfe_i32 v69, v231, s18, 1
	v_bfi_b32 v69, v69, v68, v196
	v_cndmask_b32_e64 v76, v69, v68, s[40:41]
	s_waitcnt lgkmcnt(14)
	v_mfma_f32_32x32x16_f16 v[16:31], v[144:147], v[180:183], v[16:31]
	v_exp_f32_e32 v48, v48
	v_exp_f32_e32 v49, v49
	v_exp_f32_e32 v50, v50
	v_exp_f32_e32 v51, v51
	ds_read_b128 v[156:159], v76
	ds_read_b128 v[68:71], v76 offset:128
	s_waitcnt lgkmcnt(14)
	v_mfma_f32_32x32x16_f16 v[0:15], v[144:147], v[176:179], v[0:15]
	v_exp_f32_e32 v52, v52
	v_exp_f32_e32 v53, v53
	v_exp_f32_e32 v54, v54
	v_exp_f32_e32 v55, v55
	ds_read_b128 v[168:171], v76 offset:32
	ds_read_b128 v[200:203], v76 offset:160
	v_add_u32_e32 v144, s68, v232
	ds_read_b128 v[188:191], v144
	ds_read_b128 v[148:151], v144 offset:512
	s_waitcnt lgkmcnt(14)
	v_mfma_f32_32x32x16_f16 v[16:31], v[140:143], v[172:175], v[16:31]
	v_exp_f32_e32 v56, v56
	v_exp_f32_e32 v57, v57
	v_exp_f32_e32 v58, v58
	v_exp_f32_e32 v59, v59
	ds_read_b128 v[88:91], v76 offset:64
	ds_read_b128 v[72:75], v76 offset:192
	ds_read_b128 v[184:187], v144 offset:2048
	ds_read_b128 v[172:175], v144 offset:2560
	v_mfma_f32_32x32x16_f16 v[0:15], v[140:143], v[84:87], v[0:15]
	v_exp_f32_e32 v60, v60
	v_exp_f32_e32 v61, v61
	v_exp_f32_e32 v62, v62
	v_exp_f32_e32 v63, v63
	ds_read_b128 v[92:95], v76 offset:96
	ds_read_b128 v[76:79], v76 offset:224
	ds_read_b128 v[176:179], v144 offset:4096
	ds_read_b128 v[164:167], v144 offset:4608
	s_waitcnt lgkmcnt(14)
	v_mfma_f32_32x32x16_f16 v[16:31], v[136:139], v[80:83], v[16:31]
	v_exp_f32_e32 v32, v32
	v_exp_f32_e32 v33, v33
	v_exp_f32_e32 v34, v34
	v_exp_f32_e32 v35, v35
	s_waitcnt lgkmcnt(13)
	v_pk_add_f32 v[80:81], v[156:157], v[218:219] op_sel_hi:[1,0] neg_lo:[0,1] neg_hi:[0,1]
	v_pk_add_f32 v[82:83], v[158:159], v[218:219] op_sel_hi:[1,0] neg_lo:[0,1] neg_hi:[0,1]
	s_waitcnt lgkmcnt(11)
	v_pk_add_f32 v[84:85], v[168:169], v[218:219] op_sel_hi:[1,0] neg_lo:[0,1] neg_hi:[0,1]
	v_pk_add_f32 v[86:87], v[170:171], v[218:219] op_sel_hi:[1,0] neg_lo:[0,1] neg_hi:[0,1]
	s_waitcnt lgkmcnt(3)
	ds_read_b128 v[180:183], v144 offset:6144
	ds_read_b128 v[168:171], v144 offset:6656
	v_mfma_f32_32x32x16_f16 v[0:15], v[136:139], v[160:163], v[0:15]
	v_exp_f32_e32 v36, v36
	v_exp_f32_e32 v37, v37
	v_exp_f32_e32 v38, v38
	v_exp_f32_e32 v39, v39
	v_pk_add_f32 v[88:89], v[88:89], v[218:219] op_sel_hi:[1,0] neg_lo:[0,1] neg_hi:[0,1]
	v_pk_add_f32 v[90:91], v[90:91], v[218:219] op_sel_hi:[1,0] neg_lo:[0,1] neg_hi:[0,1]
	v_pk_add_f32 v[92:93], v[92:93], v[218:219] op_sel_hi:[1,0] neg_lo:[0,1] neg_hi:[0,1]
	v_pk_add_f32 v[94:95], v[94:95], v[218:219] op_sel_hi:[1,0] neg_lo:[0,1] neg_hi:[0,1]
	s_nop 0
	v_mfma_f32_32x32x16_f16 v[16:31], v[132:135], v[64:67], v[16:31]
	v_exp_f32_e32 v40, v40
	v_exp_f32_e32 v41, v41
	v_exp_f32_e32 v42, v42
	v_exp_f32_e32 v43, v43
	v_pk_add_f32 v[64:65], v[68:69], v[218:219] op_sel_hi:[1,0] neg_lo:[0,1] neg_hi:[0,1]
	v_pk_add_f32 v[66:67], v[70:71], v[218:219] op_sel_hi:[1,0] neg_lo:[0,1] neg_hi:[0,1]
	v_pk_add_f32 v[68:69], v[200:201], v[218:219] op_sel_hi:[1,0] neg_lo:[0,1] neg_hi:[0,1]
	v_pk_add_f32 v[70:71], v[202:203], v[218:219] op_sel_hi:[1,0] neg_lo:[0,1] neg_hi:[0,1]
	s_waitcnt lgkmcnt(4)
	v_mfma_f32_32x32x16_f16 v[0:15], v[132:135], v[152:155], v[0:15]
	v_exp_f32_e32 v44, v44
	v_exp_f32_e32 v45, v45
	v_exp_f32_e32 v46, v46
	v_exp_f32_e32 v47, v47
	v_pk_add_f32 v[72:73], v[72:73], v[218:219] op_sel_hi:[1,0] neg_lo:[0,1] neg_hi:[0,1]
	v_pk_add_f32 v[74:75], v[74:75], v[218:219] op_sel_hi:[1,0] neg_lo:[0,1] neg_hi:[0,1]
	v_pk_add_f32 v[76:77], v[76:77], v[218:219] op_sel_hi:[1,0] neg_lo:[0,1] neg_hi:[0,1]
	v_pk_add_f32 v[78:79], v[78:79], v[218:219] op_sel_hi:[1,0] neg_lo:[0,1] neg_hi:[0,1]
	s_nop 0
	s_waitcnt vmcnt(2) lgkmcnt(0)
	s_barrier
	s_andn2_b64 vcc, exec, s[0:1]
	s_cbranch_vccnz .LBB0_482
	s_waitcnt lgkmcnt(0)
	ds_read_b128 v[152:155], v228 offset:49248
	ds_read_b128 v[156:159], v228 offset:49216
	ds_read_b128 v[160:163], v228 offset:49184
	ds_read_b128 v[200:203], v228 offset:49152
	s_waitcnt lgkmcnt(3)
	v_pk_mul_f32 v[30:31], v[30:31], v[154:155]
	s_waitcnt lgkmcnt(2)
	v_pk_mul_f32 v[26:27], v[26:27], v[158:159]
	s_waitcnt lgkmcnt(1)
	v_pk_mul_f32 v[22:23], v[22:23], v[162:163]
	s_waitcnt lgkmcnt(0)
	v_pk_mul_f32 v[18:19], v[18:19], v[202:203]
	v_pk_mul_f32 v[28:29], v[28:29], v[152:153]
	v_pk_mul_f32 v[24:25], v[24:25], v[156:157]
	v_pk_mul_f32 v[20:21], v[20:21], v[160:161]
	v_pk_mul_f32 v[16:17], v[16:17], v[200:201]
	v_pk_mul_f32 v[14:15], v[14:15], v[154:155]
	v_pk_mul_f32 v[10:11], v[10:11], v[158:159]
	v_pk_mul_f32 v[6:7], v[6:7], v[162:163]
	v_pk_mul_f32 v[2:3], v[2:3], v[202:203]
	v_pk_mul_f32 v[12:13], v[12:13], v[152:153]
	v_pk_mul_f32 v[8:9], v[8:9], v[156:157]
	v_pk_mul_f32 v[4:5], v[4:5], v[160:161]
	v_pk_mul_f32 v[0:1], v[0:1], v[200:201]

; #define WAIT_BAR(N) asm volatile("s_waitcnt vmcnt(" #N ") lgkmcnt(0)\n\ts_barrier" ::: "memory")
; #define RESC() do { if (resc) { asm volatile("s_waitcnt lgkmcnt(0)" ::: "memory"); \
;       _Pragma("unroll") for (int d_ = 0; d_ < 2; ++d_) _Pragma("unroll") for (int r = 0; r < 16; ++r) o[d_][r] *= wsf[crow(r, hi)]; } } while (0)
; #define ROT() do { sl_prev = sl_cur; sl_cur = sl_next; sl_next = (sl_next == (NSLOT - 1) * SLOTB) ? 0 : sl_next + SLOTB; } while (0)
; template <bool MOBA, int THRL> ...
;     ...
;     bool resc = false;
;     ...
;     int t = 1;
;     ...
;     for (; t + 5 < NT; t += 2) {
;         STEP(pB0, pB1, pA0, pA1, t, true, true, true);       WAIT_BAR(2); RESC(); ROT();
.LBB0_485:
	v_lshl_add_u32 v36, s18, 8, v234
	s_ashr_i32 s18, s18, 2
	v_bfe_i32 v37, v231, s18, 1
	v_bfi_b32 v37, v37, v36, v196
	v_cndmask_b32_e64 v44, v37, v36, s[0:1]
	s_waitcnt lgkmcnt(14)
	v_mfma_f32_32x32x16_f16 v[16:31], v[144:147], v[156:159], v[16:31]
	v_exp_f32_e32 v80, v80
	v_exp_f32_e32 v81, v81
	v_exp_f32_e32 v82, v82
	v_exp_f32_e32 v83, v83
	ds_read_b128 v[156:159], v44
	ds_read_b128 v[36:39], v44 offset:128
	s_waitcnt lgkmcnt(14)
	v_mfma_f32_32x32x16_f16 v[0:15], v[144:147], v[152:155], v[0:15]
	v_exp_f32_e32 v84, v84
	v_exp_f32_e32 v85, v85
	v_exp_f32_e32 v86, v86
	v_exp_f32_e32 v87, v87
	ds_read_b128 v[188:191], v44 offset:32
	ds_read_b128 v[198:201], v44 offset:160
	v_add_u32_e32 v144, s45, v232
	ds_read_b128 v[176:179], v144
	ds_read_b128 v[172:175], v144 offset:512
	s_waitcnt lgkmcnt(14)
	v_mfma_f32_32x32x16_f16 v[16:31], v[140:143], v[148:151], v[16:31]
	v_exp_f32_e32 v88, v88
	v_exp_f32_e32 v89, v89
	v_exp_f32_e32 v90, v90
	v_exp_f32_e32 v91, v91
	ds_read_b128 v[56:59], v44 offset:64
	ds_read_b128 v[40:43], v44 offset:192
	ds_read_b128 v[168:171], v144 offset:2048
	ds_read_b128 v[164:167], v144 offset:2560
	v_mfma_f32_32x32x16_f16 v[0:15], v[140:143], v[52:55], v[0:15]
	v_exp_f32_e32 v92, v92
	v_exp_f32_e32 v93, v93
	v_exp_f32_e32 v94, v94
	v_exp_f32_e32 v95, v95
	ds_read_b128 v[60:63], v44 offset:96
	ds_read_b128 v[44:47], v44 offset:224
	ds_read_b128 v[160:163], v144 offset:4096
	ds_read_b128 v[152:155], v144 offset:4608
	s_waitcnt lgkmcnt(14)
	v_mfma_f32_32x32x16_f16 v[16:31], v[136:139], v[48:51], v[16:31]
	v_exp_f32_e32 v64, v64
	v_exp_f32_e32 v65, v65
	v_exp_f32_e32 v66, v66
	v_exp_f32_e32 v67, v67
	s_waitcnt lgkmcnt(13)
	v_pk_add_f32 v[48:49], v[156:157], v[218:219] op_sel_hi:[1,0] neg_lo:[0,1] neg_hi:[0,1]
	v_pk_add_f32 v[50:51], v[158:159], v[218:219] op_sel_hi:[1,0] neg_lo:[0,1] neg_hi:[0,1]
	s_waitcnt lgkmcnt(11)
	v_pk_add_f32 v[52:53], v[188:189], v[218:219] op_sel_hi:[1,0] neg_lo:[0,1] neg_hi:[0,1]
	v_pk_add_f32 v[54:55], v[190:191], v[218:219] op_sel_hi:[1,0] neg_lo:[0,1] neg_hi:[0,1]
	s_waitcnt lgkmcnt(3)
	ds_read_b128 v[156:159], v144 offset:6144
	ds_read_b128 v[148:151], v144 offset:6656
	v_mfma_f32_32x32x16_f16 v[0:15], v[136:139], v[184:187], v[0:15]
	v_exp_f32_e32 v68, v68
	v_exp_f32_e32 v69, v69
	v_exp_f32_e32 v70, v70
	v_exp_f32_e32 v71, v71
	v_pk_add_f32 v[56:57], v[56:57], v[218:219] op_sel_hi:[1,0] neg_lo:[0,1] neg_hi:[0,1]
	v_pk_add_f32 v[58:59], v[58:59], v[218:219] op_sel_hi:[1,0] neg_lo:[0,1] neg_hi:[0,1]
	v_pk_add_f32 v[60:61], v[60:61], v[218:219] op_sel_hi:[1,0] neg_lo:[0,1] neg_hi:[0,1]
	v_pk_add_f32 v[62:63], v[62:63], v[218:219] op_sel_hi:[1,0] neg_lo:[0,1] neg_hi:[0,1]
	s_nop 0
	v_mfma_f32_32x32x16_f16 v[16:31], v[132:135], v[32:35], v[16:31]
	v_exp_f32_e32 v72, v72
	v_exp_f32_e32 v73, v73
	v_exp_f32_e32 v74, v74
	v_exp_f32_e32 v75, v75
	v_pk_add_f32 v[32:33], v[36:37], v[218:219] op_sel_hi:[1,0] neg_lo:[0,1] neg_hi:[0,1]
	v_pk_add_f32 v[34:35], v[38:39], v[218:219] op_sel_hi:[1,0] neg_lo:[0,1] neg_hi:[0,1]
	v_pk_add_f32 v[36:37], v[198:199], v[218:219] op_sel_hi:[1,0] neg_lo:[0,1] neg_hi:[0,1]
	v_pk_add_f32 v[38:39], v[200:201], v[218:219] op_sel_hi:[1,0] neg_lo:[0,1] neg_hi:[0,1]
	s_waitcnt lgkmcnt(4)
	v_mfma_f32_32x32x16_f16 v[0:15], v[132:135], v[180:183], v[0:15]
	v_exp_f32_e32 v76, v76
	v_exp_f32_e32 v77, v77
	v_exp_f32_e32 v78, v78
	v_exp_f32_e32 v79, v79
	v_pk_add_f32 v[40:41], v[40:41], v[218:219] op_sel_hi:[1,0] neg_lo:[0,1] neg_hi:[0,1]
	v_pk_add_f32 v[42:43], v[42:43], v[218:219] op_sel_hi:[1,0] neg_lo:[0,1] neg_hi:[0,1]
	v_pk_add_f32 v[44:45], v[44:45], v[218:219] op_sel_hi:[1,0] neg_lo:[0,1] neg_hi:[0,1]
	v_pk_add_f32 v[46:47], v[46:47], v[218:219] op_sel_hi:[1,0] neg_lo:[0,1] neg_hi:[0,1]
	s_nop 0
	s_waitcnt vmcnt(2) lgkmcnt(0)
	s_barrier
	s_andn2_b64 vcc, exec, s[40:41]
	s_cbranch_vccnz .LBB0_487
	s_waitcnt lgkmcnt(0)
	ds_read_b128 v[180:183], v228 offset:49248
	ds_read_b128 v[184:187], v228 offset:49216
	ds_read_b128 v[188:191], v228 offset:49184
	ds_read_b128 v[198:201], v228 offset:49152
	s_waitcnt lgkmcnt(3)
	v_pk_mul_f32 v[30:31], v[30:31], v[182:183]
	s_waitcnt lgkmcnt(2)
	v_pk_mul_f32 v[26:27], v[26:27], v[186:187]
	s_waitcnt lgkmcnt(1)
	v_pk_mul_f32 v[22:23], v[22:23], v[190:191]
	s_waitcnt lgkmcnt(0)
	v_pk_mul_f32 v[18:19], v[18:19], v[200:201]
	v_pk_mul_f32 v[28:29], v[28:29], v[180:181]
	v_pk_mul_f32 v[24:25], v[24:25], v[184:185]
	v_pk_mul_f32 v[20:21], v[20:21], v[188:189]
	v_pk_mul_f32 v[16:17], v[16:17], v[198:199]
	v_pk_mul_f32 v[14:15], v[14:15], v[182:183]
	v_pk_mul_f32 v[10:11], v[10:11], v[186:187]
	v_pk_mul_f32 v[6:7], v[6:7], v[190:191]
	v_pk_mul_f32 v[2:3], v[2:3], v[200:201]
	v_pk_mul_f32 v[12:13], v[12:13], v[180:181]
	v_pk_mul_f32 v[8:9], v[8:9], v[184:185]
	v_pk_mul_f32 v[4:5], v[4:5], v[188:189]
	v_pk_mul_f32 v[0:1], v[0:1], v[198:199]
